# baseline (speedup 1.0000x reference)
_Z12score_kernelPKfP15HIP_vector_typeIjLj2EES0_S0_:
	s_load_dwordx4 s[4:7], s[0:1], 0x0
	s_load_dwordx4 s[32:35], s[0:1], 0x10
	s_and_b32 s15, s2, 7
	s_lshl_b32 s15, s15, 2
	s_lshr_b32 s17, s2, 6
	s_add_u32 s15, s15, s17
	s_bfe_u32 s16, s2, 0x30003
	s_mul_i32 s17, s16, 0x271
	s_lshr_b32 s28, s17, 1
	v_lshrrev_b32_e32 v3, 1, v0
	v_and_b32_e32 v3, 0x3e0, v3
	v_and_or_b32 v3, v0, 31, v3
	v_bfe_u32 v96, v0, 5, 1
	v_add_u32_e32 v2, s28, v3
	v_lshlrev_b32_e32 v1, 3, v2
	v_lshl_add_u32 v2, v2, 1, v96
	s_movk_i32 s29, 0x4e20
	v_mad_u32_u24 v1, v96, s29, v1
	v_lshlrev_b32_e32 v99, 2, v2
	s_movk_i32 s3, 0x139
	v_cmp_gt_u32_e32 vcc, s3, v3
	v_readfirstlane_b32 s21, v0
	s_and_b64 exec, exec, vcc
	s_mov_b64 s[18:19], exec
	v_subrev_u32_e32 v97, s17, v2
	s_movk_i32 s3, 0x271
	v_cmp_gt_u32_e64 s[24:25], s3, v97
	s_lshr_b32 s21, s21, 6
	s_movk_i32 s13, 0x4e20
	s_mov_b32 s14, 0x3fb8aa3b
	s_mov_b32 s12, 0
	s_mov_b32 s10, 0x13d620
	s_mov_b32 s11, 0x20000
	s_mul_i32 s17, s15, 0x13d620
	s_mul_hi_u32 s20, s15, 0x13d620
	s_mov_b32 s40, 0
	s_add_u32 s41, s40, s13
	s_add_u32 s42, s41, s13
	s_add_u32 s43, s42, s13
	s_add_u32 s44, s43, s13
	s_add_u32 s45, s44, s13
	s_add_u32 s46, s45, s13
	s_add_u32 s47, s46, s13
	s_add_u32 s48, s47, s13
	s_add_u32 s49, s48, s13
	s_add_u32 s50, s49, s13
	s_add_u32 s51, s50, s13
	s_add_u32 s52, s51, s13
	s_add_u32 s53, s52, s13
	s_add_u32 s54, s53, s13
	s_add_u32 s55, s54, s13
	s_cmp_lg_u32 s21, 0
	s_cbranch_scc1 .Lk1_nowarm0
	s_getpc_b64 s[30:31]
	v_lshlrev_b32_e32 v3, 6, v0
	global_load_dword v92, v3, s[30:31]
	s_add_u32 s30, s30, 0x1000
	s_addc_u32 s31, s31, 0
	global_load_dword v93, v3, s[30:31]
	s_add_u32 s30, s30, 0x1000
	s_addc_u32 s31, s31, 0
	global_load_dword v94, v3, s[30:31]
	s_and_b32 s30, s0, 0xfffff000
	s_mov_b32 s31, s1
	global_load_dword v95, v3, s[30:31]

.Lk1_nowarm9:
	buffer_load_dwordx2 v[8:9], v1, s[8:11], s40 offen nt
	buffer_load_dwordx2 v[10:11], v1, s[8:11], s42 offen nt
	buffer_load_dwordx2 v[12:13], v1, s[8:11], s44 offen nt
	buffer_load_dwordx2 v[14:15], v1, s[8:11], s46 offen nt
	buffer_load_dwordx2 v[16:17], v1, s[8:11], s48 offen nt
	buffer_load_dwordx2 v[18:19], v1, s[8:11], s50 offen nt
	buffer_load_dwordx2 v[20:21], v1, s[8:11], s52 offen nt
	buffer_load_dwordx2 v[22:23], v1, s[8:11], s54 offen nt
	s_add_u32 s8, s8, 0x4e200
	s_addc_u32 s9, s9, 0
	buffer_load_dwordx2 v[24:25], v1, s[8:11], s40 offen nt
	buffer_load_dwordx2 v[26:27], v1, s[8:11], s42 offen nt
	buffer_load_dwordx2 v[28:29], v1, s[8:11], s44 offen nt
	buffer_load_dwordx2 v[30:31], v1, s[8:11], s46 offen nt
	buffer_load_dwordx2 v[32:33], v1, s[8:11], s48 offen nt
	buffer_load_dwordx2 v[34:35], v1, s[8:11], s50 offen nt
	buffer_load_dwordx2 v[36:37], v1, s[8:11], s52 offen nt
	buffer_load_dwordx2 v[38:39], v1, s[8:11], s54 offen nt
	s_add_u32 s8, s8, 0x4e200
	s_addc_u32 s9, s9, 0
	buffer_load_dwordx2 v[40:41], v1, s[8:11], s40 offen nt
	buffer_load_dwordx2 v[42:43], v1, s[8:11], s42 offen nt
	buffer_load_dwordx2 v[44:45], v1, s[8:11], s44 offen nt
	buffer_load_dwordx2 v[46:47], v1, s[8:11], s46 offen nt
	buffer_load_dwordx2 v[48:49], v1, s[8:11], s48 offen nt
	buffer_load_dwordx2 v[50:51], v1, s[8:11], s50 offen nt
	buffer_load_dwordx2 v[52:53], v1, s[8:11], s52 offen nt
	buffer_load_dwordx2 v[54:55], v1, s[8:11], s54 offen nt
	s_add_u32 s8, s8, 0x4e200
	s_addc_u32 s9, s9, 0
	buffer_load_dwordx2 v[56:57], v1, s[8:11], s40 offen nt
	buffer_load_dwordx2 v[58:59], v1, s[8:11], s42 offen nt
	buffer_load_dwordx2 v[60:61], v1, s[8:11], s44 offen nt
	buffer_load_dwordx2 v[62:63], v1, s[8:11], s46 offen nt
	buffer_load_dwordx2 v[64:65], v1, s[8:11], s48 offen nt
	buffer_load_dwordx2 v[66:67], v1, s[8:11], s50 offen nt
	buffer_load_dwordx2 v[68:69], v1, s[8:11], s52 offen nt
	buffer_load_dwordx2 v[70:71], v1, s[8:11], s54 offen nt
	s_add_u32 s8, s8, 0x4e200
	s_addc_u32 s9, s9, 0
	buffer_load_dword v72, v99, s[8:11], s40 offen nt
	v_mul_u32_u24_e32 v3, 0x147b, v2
	v_lshrrev_b32_e32 v3, 19, v3
	v_mul_u32_u24_e32 v98, 0x64, v3
	v_sub_u32_e32 v98, v2, v98
	v_add_u32_e32 v3, -1, v3
	v_add_u32_e32 v98, -1, v98
	s_movk_i32 s17, 0x62
	v_cmp_gt_u32_e64 s[36:37], 48, v3
	v_cmp_gt_u32_e64 s[38:39], s17, v98
	s_mul_i32 s17, s15, 0x1388
	v_add_lshl_u32 v98, v2, s17, 3
	s_and_b64 s[36:37], s[36:37], s[38:39]
	s_waitcnt vmcnt(25)
	v_permlane32_swap_b32_e32 v8, v9
	v_permlane32_swap_b32_e32 v10, v11
	v_permlane32_swap_b32_e32 v12, v13
	v_permlane32_swap_b32_e32 v14, v15
	v_permlane32_swap_b32_e32 v16, v17
	v_permlane32_swap_b32_e32 v18, v19
	v_permlane32_swap_b32_e32 v20, v21
	v_permlane32_swap_b32_e32 v22, v23
	v_max3_f32 v76, v8, v9, v10
	v_max3_f32 v76, v76, v11, v12
	v_max3_f32 v76, v76, v13, v14
	v_max3_f32 v76, v76, v15, v16
	v_max3_f32 v76, v76, v17, v18
	v_max3_f32 v76, v76, v19, v20
	v_max3_f32 v76, v76, v21, v22
	v_max_f32_e32 v76, v76, v23
	v_pk_add_f32 v[8:9], v[8:9], v[76:77] op_sel_hi:[1,0] neg_lo:[0,1] neg_hi:[0,1]
	v_pk_add_f32 v[10:11], v[10:11], v[76:77] op_sel_hi:[1,0] neg_lo:[0,1] neg_hi:[0,1]
	v_pk_add_f32 v[12:13], v[12:13], v[76:77] op_sel_hi:[1,0] neg_lo:[0,1] neg_hi:[0,1]
	v_pk_add_f32 v[14:15], v[14:15], v[76:77] op_sel_hi:[1,0] neg_lo:[0,1] neg_hi:[0,1]
	v_pk_add_f32 v[16:17], v[16:17], v[76:77] op_sel_hi:[1,0] neg_lo:[0,1] neg_hi:[0,1]
	v_pk_add_f32 v[18:19], v[18:19], v[76:77] op_sel_hi:[1,0] neg_lo:[0,1] neg_hi:[0,1]
	v_pk_add_f32 v[20:21], v[20:21], v[76:77] op_sel_hi:[1,0] neg_lo:[0,1] neg_hi:[0,1]
	v_pk_add_f32 v[22:23], v[22:23], v[76:77] op_sel_hi:[1,0] neg_lo:[0,1] neg_hi:[0,1]
	v_or_b32_e32 v81, 0, v8
	v_or_b32_e32 v82, 1, v9
	v_min_u32_e32 v80, v81, v82
	v_or_b32_e32 v81, 2, v10
	v_or_b32_e32 v82, 3, v11
	v_min3_u32 v80, v80, v81, v82
	v_or_b32_e32 v81, 4, v12
	v_or_b32_e32 v82, 5, v13
	v_min3_u32 v80, v80, v81, v82
	v_or_b32_e32 v81, 6, v14
	v_or_b32_e32 v82, 7, v15
	v_min3_u32 v80, v80, v81, v82
	v_or_b32_e32 v81, 8, v16
	v_or_b32_e32 v82, 9, v17
	v_min3_u32 v80, v80, v81, v82
	v_or_b32_e32 v81, 10, v18
	v_or_b32_e32 v82, 11, v19
	v_min3_u32 v80, v80, v81, v82
	v_or_b32_e32 v81, 12, v20
	v_or_b32_e32 v82, 13, v21
	v_min3_u32 v80, v80, v81, v82
	v_or_b32_e32 v81, 14, v22
	v_or_b32_e32 v82, 15, v23
	v_min3_u32 v80, v80, v81, v82
	v_pk_mul_f32 v[8:9], v[8:9], s[14:15] op_sel_hi:[1,0]
	v_pk_mul_f32 v[10:11], v[10:11], s[14:15] op_sel_hi:[1,0]
	v_pk_mul_f32 v[12:13], v[12:13], s[14:15] op_sel_hi:[1,0]
	v_pk_mul_f32 v[14:15], v[14:15], s[14:15] op_sel_hi:[1,0]
	v_pk_mul_f32 v[16:17], v[16:17], s[14:15] op_sel_hi:[1,0]
	v_pk_mul_f32 v[18:19], v[18:19], s[14:15] op_sel_hi:[1,0]
	v_pk_mul_f32 v[20:21], v[20:21], s[14:15] op_sel_hi:[1,0]
	v_pk_mul_f32 v[22:23], v[22:23], s[14:15] op_sel_hi:[1,0]
	v_exp_f32_e32 v8, v8
	v_exp_f32_e32 v9, v9
	v_exp_f32_e32 v10, v10
	v_exp_f32_e32 v11, v11
	v_exp_f32_e32 v12, v12
	v_exp_f32_e32 v13, v13
	v_exp_f32_e32 v14, v14
	v_exp_f32_e32 v15, v15
	v_exp_f32_e32 v16, v16
	v_exp_f32_e32 v17, v17
	v_exp_f32_e32 v18, v18
	v_exp_f32_e32 v19, v19
	v_exp_f32_e32 v20, v20
	v_exp_f32_e32 v21, v21
	v_exp_f32_e32 v22, v22
	v_exp_f32_e32 v23, v23
	v_pk_add_f32 v[78:79], v[8:9], v[10:11]
	v_pk_add_f32 v[78:79], v[78:79], v[12:13]
	v_pk_add_f32 v[78:79], v[78:79], v[14:15]
	v_pk_add_f32 v[78:79], v[78:79], v[16:17]
	v_pk_add_f32 v[78:79], v[78:79], v[18:19]
	v_pk_add_f32 v[78:79], v[78:79], v[20:21]
	v_pk_add_f32 v[78:79], v[78:79], v[22:23]
	v_add_f32_e32 v78, v78, v79
	v_cvt_f64_f32_e32 v[86:87], v78
	v_mov_b32_e32 v75, v80
	v_mov_b32_e32 v73, v76
	s_waitcnt vmcnt(17)
	v_permlane32_swap_b32_e32 v24, v25
	v_permlane32_swap_b32_e32 v26, v27
	v_permlane32_swap_b32_e32 v28, v29
	v_permlane32_swap_b32_e32 v30, v31
	v_permlane32_swap_b32_e32 v32, v33
	v_permlane32_swap_b32_e32 v34, v35
	v_permlane32_swap_b32_e32 v36, v37
	v_permlane32_swap_b32_e32 v38, v39
	v_max3_f32 v76, v24, v25, v26
	v_max3_f32 v76, v76, v27, v28
	v_max3_f32 v76, v76, v29, v30
	v_max3_f32 v76, v76, v31, v32
	v_max3_f32 v76, v76, v33, v34
	v_max3_f32 v76, v76, v35, v36
	v_max3_f32 v76, v76, v37, v38
	v_max_f32_e32 v76, v76, v39
	v_max_f32_e32 v100, v73, v76
	v_cmp_gt_f32_e64 s[26:27], v76, v73
	v_sub_f32_e32 v83, v73, v100
	v_mul_f32_e32 v83, s14, v83
	v_exp_f32_e32 v83, v83
	v_pk_add_f32 v[24:25], v[24:25], v[100:101] op_sel_hi:[1,0] neg_lo:[0,1] neg_hi:[0,1]
	v_pk_add_f32 v[26:27], v[26:27], v[100:101] op_sel_hi:[1,0] neg_lo:[0,1] neg_hi:[0,1]
	v_pk_add_f32 v[28:29], v[28:29], v[100:101] op_sel_hi:[1,0] neg_lo:[0,1] neg_hi:[0,1]
	v_pk_add_f32 v[30:31], v[30:31], v[100:101] op_sel_hi:[1,0] neg_lo:[0,1] neg_hi:[0,1]
	v_pk_add_f32 v[32:33], v[32:33], v[100:101] op_sel_hi:[1,0] neg_lo:[0,1] neg_hi:[0,1]
	v_pk_add_f32 v[34:35], v[34:35], v[100:101] op_sel_hi:[1,0] neg_lo:[0,1] neg_hi:[0,1]
	v_pk_add_f32 v[36:37], v[36:37], v[100:101] op_sel_hi:[1,0] neg_lo:[0,1] neg_hi:[0,1]
	v_pk_add_f32 v[38:39], v[38:39], v[100:101] op_sel_hi:[1,0] neg_lo:[0,1] neg_hi:[0,1]
	v_cvt_f64_f32_e32 v[90:91], v83
	v_or_b32_e32 v81, 16, v24
	v_or_b32_e32 v82, 17, v25
	v_min_u32_e32 v80, v81, v82
	v_or_b32_e32 v81, 18, v26
	v_or_b32_e32 v82, 19, v27
	v_min3_u32 v80, v80, v81, v82
	v_or_b32_e32 v81, 20, v28
	v_or_b32_e32 v82, 21, v29
	v_min3_u32 v80, v80, v81, v82
	v_or_b32_e32 v81, 22, v30
	v_or_b32_e32 v82, 23, v31
	v_min3_u32 v80, v80, v81, v82
	v_or_b32_e32 v81, 24, v32
	v_or_b32_e32 v82, 25, v33
	v_min3_u32 v80, v80, v81, v82
	v_or_b32_e32 v81, 26, v34
	v_or_b32_e32 v82, 27, v35
	v_min3_u32 v80, v80, v81, v82
	v_or_b32_e32 v81, 28, v36
	v_or_b32_e32 v82, 29, v37
	v_min3_u32 v80, v80, v81, v82
	v_or_b32_e32 v81, 30, v38
	v_or_b32_e32 v82, 31, v39
	v_min3_u32 v80, v80, v81, v82
	v_pk_mul_f32 v[24:25], v[24:25], s[14:15] op_sel_hi:[1,0]
	v_pk_mul_f32 v[26:27], v[26:27], s[14:15] op_sel_hi:[1,0]
	v_pk_mul_f32 v[28:29], v[28:29], s[14:15] op_sel_hi:[1,0]
	v_pk_mul_f32 v[30:31], v[30:31], s[14:15] op_sel_hi:[1,0]
	v_pk_mul_f32 v[32:33], v[32:33], s[14:15] op_sel_hi:[1,0]
	v_pk_mul_f32 v[34:35], v[34:35], s[14:15] op_sel_hi:[1,0]
	v_pk_mul_f32 v[36:37], v[36:37], s[14:15] op_sel_hi:[1,0]
	v_pk_mul_f32 v[38:39], v[38:39], s[14:15] op_sel_hi:[1,0]
	v_exp_f32_e32 v24, v24
	v_exp_f32_e32 v25, v25
	v_exp_f32_e32 v26, v26
	v_exp_f32_e32 v27, v27
	v_exp_f32_e32 v28, v28
	v_exp_f32_e32 v29, v29
	v_exp_f32_e32 v30, v30
	v_exp_f32_e32 v31, v31
	v_exp_f32_e32 v32, v32
	v_exp_f32_e32 v33, v33
	v_exp_f32_e32 v34, v34
	v_exp_f32_e32 v35, v35
	v_exp_f32_e32 v36, v36
	v_exp_f32_e32 v37, v37
	v_exp_f32_e32 v38, v38
	v_exp_f32_e32 v39, v39
	v_pk_add_f32 v[78:79], v[24:25], v[26:27]
	v_pk_add_f32 v[78:79], v[78:79], v[28:29]
	v_pk_add_f32 v[78:79], v[78:79], v[30:31]
	v_pk_add_f32 v[78:79], v[78:79], v[32:33]
	v_pk_add_f32 v[78:79], v[78:79], v[34:35]
	v_pk_add_f32 v[78:79], v[78:79], v[36:37]
	v_pk_add_f32 v[78:79], v[78:79], v[38:39]
	v_add_f32_e32 v78, v78, v79
	v_cvt_f64_f32_e32 v[84:85], v78
	v_cndmask_b32_e64 v75, v75, v80, s[26:27]
	v_mov_b32_e32 v73, v100
	v_fma_f64 v[86:87], v[86:87], v[90:91], v[84:85]
	s_waitcnt vmcnt(9)
	v_permlane32_swap_b32_e32 v40, v41
	v_permlane32_swap_b32_e32 v42, v43
	v_permlane32_swap_b32_e32 v44, v45
	v_permlane32_swap_b32_e32 v46, v47
	v_permlane32_swap_b32_e32 v48, v49
	v_permlane32_swap_b32_e32 v50, v51
	v_permlane32_swap_b32_e32 v52, v53
	v_permlane32_swap_b32_e32 v54, v55
	v_max3_f32 v76, v40, v41, v42
	v_max3_f32 v76, v76, v43, v44
	v_max3_f32 v76, v76, v45, v46
	v_max3_f32 v76, v76, v47, v48
	v_max3_f32 v76, v76, v49, v50
	v_max3_f32 v76, v76, v51, v52
	v_max3_f32 v76, v76, v53, v54
	v_max_f32_e32 v76, v76, v55
	v_max_f32_e32 v100, v73, v76
	v_cmp_gt_f32_e64 s[26:27], v76, v73
	v_sub_f32_e32 v83, v73, v100
	v_mul_f32_e32 v83, s14, v83
	v_exp_f32_e32 v83, v83
	v_pk_add_f32 v[40:41], v[40:41], v[100:101] op_sel_hi:[1,0] neg_lo:[0,1] neg_hi:[0,1]
	v_pk_add_f32 v[42:43], v[42:43], v[100:101] op_sel_hi:[1,0] neg_lo:[0,1] neg_hi:[0,1]
	v_pk_add_f32 v[44:45], v[44:45], v[100:101] op_sel_hi:[1,0] neg_lo:[0,1] neg_hi:[0,1]
	v_pk_add_f32 v[46:47], v[46:47], v[100:101] op_sel_hi:[1,0] neg_lo:[0,1] neg_hi:[0,1]
	v_pk_add_f32 v[48:49], v[48:49], v[100:101] op_sel_hi:[1,0] neg_lo:[0,1] neg_hi:[0,1]
	v_pk_add_f32 v[50:51], v[50:51], v[100:101] op_sel_hi:[1,0] neg_lo:[0,1] neg_hi:[0,1]
	v_pk_add_f32 v[52:53], v[52:53], v[100:101] op_sel_hi:[1,0] neg_lo:[0,1] neg_hi:[0,1]
	v_pk_add_f32 v[54:55], v[54:55], v[100:101] op_sel_hi:[1,0] neg_lo:[0,1] neg_hi:[0,1]
	v_cvt_f64_f32_e32 v[90:91], v83
	v_or_b32_e32 v81, 32, v40
	v_or_b32_e32 v82, 33, v41
	v_min_u32_e32 v80, v81, v82
	v_or_b32_e32 v81, 34, v42
	v_or_b32_e32 v82, 35, v43
	v_min3_u32 v80, v80, v81, v82
	v_or_b32_e32 v81, 36, v44
	v_or_b32_e32 v82, 37, v45
	v_min3_u32 v80, v80, v81, v82
	v_or_b32_e32 v81, 38, v46
	v_or_b32_e32 v82, 39, v47
	v_min3_u32 v80, v80, v81, v82
	v_or_b32_e32 v81, 40, v48
	v_or_b32_e32 v82, 41, v49
	v_min3_u32 v80, v80, v81, v82
	v_or_b32_e32 v81, 42, v50
	v_or_b32_e32 v82, 43, v51
	v_min3_u32 v80, v80, v81, v82
	v_or_b32_e32 v81, 44, v52
	v_or_b32_e32 v82, 45, v53
	v_min3_u32 v80, v80, v81, v82
	v_or_b32_e32 v81, 46, v54
	v_or_b32_e32 v82, 47, v55
	v_min3_u32 v80, v80, v81, v82
	v_pk_mul_f32 v[40:41], v[40:41], s[14:15] op_sel_hi:[1,0]
	v_pk_mul_f32 v[42:43], v[42:43], s[14:15] op_sel_hi:[1,0]
	v_pk_mul_f32 v[44:45], v[44:45], s[14:15] op_sel_hi:[1,0]
	v_pk_mul_f32 v[46:47], v[46:47], s[14:15] op_sel_hi:[1,0]
	v_pk_mul_f32 v[48:49], v[48:49], s[14:15] op_sel_hi:[1,0]
	v_pk_mul_f32 v[50:51], v[50:51], s[14:15] op_sel_hi:[1,0]
	v_pk_mul_f32 v[52:53], v[52:53], s[14:15] op_sel_hi:[1,0]
	v_pk_mul_f32 v[54:55], v[54:55], s[14:15] op_sel_hi:[1,0]
	v_exp_f32_e32 v40, v40
	v_exp_f32_e32 v41, v41
	v_exp_f32_e32 v42, v42
	v_exp_f32_e32 v43, v43
	v_exp_f32_e32 v44, v44
	v_exp_f32_e32 v45, v45
	v_exp_f32_e32 v46, v46
	v_exp_f32_e32 v47, v47
	v_exp_f32_e32 v48, v48
	v_exp_f32_e32 v49, v49
	v_exp_f32_e32 v50, v50
	v_exp_f32_e32 v51, v51
	v_exp_f32_e32 v52, v52
	v_exp_f32_e32 v53, v53
	v_exp_f32_e32 v54, v54
	v_exp_f32_e32 v55, v55
	v_pk_add_f32 v[78:79], v[40:41], v[42:43]
	v_pk_add_f32 v[78:79], v[78:79], v[44:45]
	v_pk_add_f32 v[78:79], v[78:79], v[46:47]
	v_pk_add_f32 v[78:79], v[78:79], v[48:49]
	v_pk_add_f32 v[78:79], v[78:79], v[50:51]
	v_pk_add_f32 v[78:79], v[78:79], v[52:53]
	v_pk_add_f32 v[78:79], v[78:79], v[54:55]
	v_add_f32_e32 v78, v78, v79
	v_cvt_f64_f32_e32 v[84:85], v78
	v_cndmask_b32_e64 v75, v75, v80, s[26:27]
	v_mov_b32_e32 v73, v100
	v_fma_f64 v[86:87], v[86:87], v[90:91], v[84:85]
	s_waitcnt vmcnt(5)
	v_permlane32_swap_b32_e32 v56, v57
	v_permlane32_swap_b32_e32 v58, v59
	v_permlane32_swap_b32_e32 v60, v61
	v_permlane32_swap_b32_e32 v62, v63
	v_max3_f32 v76, v56, v57, v58
	v_max3_f32 v76, v76, v59, v60
	v_max3_f32 v76, v76, v61, v62
	v_max_f32_e32 v76, v76, v63
	v_max_f32_e32 v100, v73, v76
	v_cmp_gt_f32_e64 s[26:27], v76, v73
	v_sub_f32_e32 v83, v73, v100
	v_mul_f32_e32 v83, s14, v83
	v_exp_f32_e32 v83, v83
	v_pk_add_f32 v[56:57], v[56:57], v[100:101] op_sel_hi:[1,0] neg_lo:[0,1] neg_hi:[0,1]
	v_pk_add_f32 v[58:59], v[58:59], v[100:101] op_sel_hi:[1,0] neg_lo:[0,1] neg_hi:[0,1]
	v_pk_add_f32 v[60:61], v[60:61], v[100:101] op_sel_hi:[1,0] neg_lo:[0,1] neg_hi:[0,1]
	v_pk_add_f32 v[62:63], v[62:63], v[100:101] op_sel_hi:[1,0] neg_lo:[0,1] neg_hi:[0,1]
	v_cvt_f64_f32_e32 v[90:91], v83
	v_or_b32_e32 v81, 48, v56
	v_or_b32_e32 v82, 49, v57
	v_min_u32_e32 v80, v81, v82
	v_or_b32_e32 v81, 50, v58
	v_or_b32_e32 v82, 51, v59
	v_min3_u32 v80, v80, v81, v82
	v_or_b32_e32 v81, 52, v60
	v_or_b32_e32 v82, 53, v61
	v_min3_u32 v80, v80, v81, v82
	v_or_b32_e32 v81, 54, v62
	v_or_b32_e32 v82, 55, v63
	v_min3_u32 v80, v80, v81, v82
	v_pk_mul_f32 v[56:57], v[56:57], s[14:15] op_sel_hi:[1,0]
	v_pk_mul_f32 v[58:59], v[58:59], s[14:15] op_sel_hi:[1,0]
	v_pk_mul_f32 v[60:61], v[60:61], s[14:15] op_sel_hi:[1,0]
	v_pk_mul_f32 v[62:63], v[62:63], s[14:15] op_sel_hi:[1,0]
	v_exp_f32_e32 v56, v56
	v_exp_f32_e32 v57, v57
	v_exp_f32_e32 v58, v58
	v_exp_f32_e32 v59, v59
	v_exp_f32_e32 v60, v60
	v_exp_f32_e32 v61, v61
	v_exp_f32_e32 v62, v62
	v_exp_f32_e32 v63, v63
	v_pk_add_f32 v[78:79], v[56:57], v[58:59]
	v_pk_add_f32 v[78:79], v[78:79], v[60:61]
	v_pk_add_f32 v[78:79], v[78:79], v[62:63]
	v_add_f32_e32 v78, v78, v79
	v_cvt_f64_f32_e32 v[84:85], v78
	v_cndmask_b32_e64 v75, v75, v80, s[26:27]
	v_mov_b32_e32 v73, v100
	v_fma_f64 v[86:87], v[86:87], v[90:91], v[84:85]
	s_waitcnt vmcnt(3)
	v_permlane32_swap_b32_e32 v64, v65
	v_permlane32_swap_b32_e32 v66, v67
	v_max3_f32 v76, v64, v65, v66
	v_max_f32_e32 v76, v76, v67
	v_max_f32_e32 v100, v73, v76
	v_cmp_gt_f32_e64 s[26:27], v76, v73
	v_sub_f32_e32 v83, v73, v100
	v_mul_f32_e32 v83, s14, v83
	v_exp_f32_e32 v83, v83
	v_pk_add_f32 v[64:65], v[64:65], v[100:101] op_sel_hi:[1,0] neg_lo:[0,1] neg_hi:[0,1]
	v_pk_add_f32 v[66:67], v[66:67], v[100:101] op_sel_hi:[1,0] neg_lo:[0,1] neg_hi:[0,1]
	v_cvt_f64_f32_e32 v[90:91], v83
	v_or_b32_e32 v81, 56, v64
	v_or_b32_e32 v82, 57, v65
	v_min_u32_e32 v80, v81, v82
	v_or_b32_e32 v81, 58, v66
	v_or_b32_e32 v82, 59, v67
	v_min3_u32 v80, v80, v81, v82
	v_pk_mul_f32 v[64:65], v[64:65], s[14:15] op_sel_hi:[1,0]
	v_pk_mul_f32 v[66:67], v[66:67], s[14:15] op_sel_hi:[1,0]
	v_exp_f32_e32 v64, v64
	v_exp_f32_e32 v65, v65
	v_exp_f32_e32 v66, v66
	v_exp_f32_e32 v67, v67
	s_nop 0
	v_pk_add_f32 v[78:79], v[64:65], v[66:67]
	v_add_f32_e32 v78, v78, v79
	v_cvt_f64_f32_e32 v[84:85], v78
	v_cndmask_b32_e64 v75, v75, v80, s[26:27]
	v_mov_b32_e32 v73, v100
	v_fma_f64 v[86:87], v[86:87], v[90:91], v[84:85]
	s_waitcnt vmcnt(0)
	v_permlane32_swap_b32_e32 v68, v69
	v_permlane32_swap_b32_e32 v70, v71
	v_max3_f32 v76, v68, v69, v70
	v_max3_f32 v76, v76, v71, v72
	v_max_f32_e32 v100, v73, v76
	v_cmp_gt_f32_e64 s[26:27], v76, v73
	v_sub_f32_e32 v83, v73, v100
	v_mul_f32_e32 v83, s14, v83
	v_exp_f32_e32 v83, v83
	v_pk_add_f32 v[68:69], v[68:69], v[100:101] op_sel_hi:[1,0] neg_lo:[0,1] neg_hi:[0,1]
	v_pk_add_f32 v[70:71], v[70:71], v[100:101] op_sel_hi:[1,0] neg_lo:[0,1] neg_hi:[0,1]
	v_sub_f32_e32 v72, v72, v100
	v_cvt_f64_f32_e32 v[90:91], v83
	v_or_b32_e32 v81, 60, v68
	v_or_b32_e32 v82, 61, v69
	v_min_u32_e32 v80, v81, v82
	v_or_b32_e32 v81, 62, v70
	v_or_b32_e32 v82, 63, v71
	v_min3_u32 v80, v80, v81, v82
	v_or_b32_e32 v81, 64, v72
	v_min_u32_e32 v80, v80, v81
	v_pk_mul_f32 v[68:69], v[68:69], s[14:15] op_sel_hi:[1,0]
	v_pk_mul_f32 v[70:71], v[70:71], s[14:15] op_sel_hi:[1,0]
	v_mul_f32_e32 v72, s14, v72
	v_exp_f32_e32 v68, v68
	v_exp_f32_e32 v69, v69
	v_exp_f32_e32 v70, v70
	v_exp_f32_e32 v71, v71
	v_exp_f32_e32 v72, v72
	v_cndmask_b32_e64 v75, v75, v80, s[26:27]
	v_pk_add_f32 v[78:79], v[68:69], v[70:71]
	v_add_f32_e32 v78, v78, v79
	v_add_f32_e32 v78, v78, v72
	v_cvt_f64_f32_e32 v[84:85], v78
	v_fma_f64 v[86:87], v[86:87], v[90:91], v[84:85]
	v_rcp_f64_e32 v[88:89], v[86:87]
	v_cmp_gt_u32_e32 vcc, 64, v75
	s_and_b64 vcc, vcc, s[36:37]
	v_fma_f64 v[90:91], -v[86:87], v[88:89], 1.0
	v_fma_f64 v[88:89], v[90:91], v[88:89], v[88:89]
	v_cvt_f32_f64_e32 v3, v[88:89]
	v_cndmask_b32_e32 v74, 0, v3, vcc
	s_and_b64 exec, exec, s[24:25]
	global_store_dwordx2 v98, v[74:75], s[6:7]
